# outproj (both layers): tile index starts from bid with its low 3-bit fields swapped so the 8 N-tiles of an M-tile run on one XCD
# speedup vs baseline: 1.0129x; 1.0122x over previous
;     template <int BM> __device__ __forceinline__ void init(const bfr* base, int ld, int row0, int maxrow, const int* ridx) {
; #pragma unroll
;         for (int i = 0; i < (BM * 4 + NTHR - 1) / NTHR; ++i) {
;             const int id = threadIdx.x + i * NTHR, kc = id & 3;
;             int r = id >> 2; if (r > BM - 1) r = BM - 1;
;             int row = ridx ? ridx[r] : row0 + r;
;             if (row > maxrow) row = maxrow;
;             p[i] = base + (size_t)row * ld + kc * 8;
;         }
;     }
;     template <int BN> __device__ __forceinline__ void init(const bfr* base, int ld, int n0) {
; #pragma unroll
;         for (int i = 0; i < BN * 4 / NTHR; ++i) {
;             const int id = threadIdx.x + i * NTHR, r = id >> 2, kc = id & 3;
;             p[i] = base + (size_t)(n0 + r) * ld + kc * 8;
;         }
;     }
; __device__ __forceinline__ void phase_outproj(const Params& P, int layer, bfr* smem, int bid, int nb) {
;     ...
;     const int mt = (M + 255) / 256, nu = mt * 8;
;     GemmPipe<256, 128, 1024, ALoadRows, BLoadT> gp;
;     ALoadRows al; BLoadT bl;
;     int u = bid;
;     if (u < nu) { al.init<256>(A, 1024, m0 + (u >> 3) * 256, NT - 1, nullptr); bl.init<128>(Bt, 1024, (u & 7) * 128); gp.prefetch(al, bl); }
;     while (u < nu) {
;         EpiOutProj ep{xc, xl, x2, mod, (bfr*)(P.ws + WS_PRE), m0 + (u >> 3) * 256, (u & 7) * 128};
;         gp.mainloop(smem, al, bl);
;         const int un = u + nb;
;         if (un < nu) { al.init<256>(A, 1024, m0 + (un >> 3) * 256, NT - 1, nullptr); bl.init<128>(Bt, 1024, (un & 7) * 128); gp.prefetch(al, bl); }
.LBB0_973:
	s_cmp_lt_i32 s6, 6
	s_cselect_b64 s[0:1], -1, 0
	s_cmp_gt_i32 s7, 5
	s_cselect_b64 s[2:3], -1, 0
	s_and_b64 s[0:1], s[0:1], s[2:3]
	s_andn2_b64 vcc, exec, s[0:1]
	s_cbranch_vccnz .LBB0_1041
	v_readlane_b32 s96, v253, 10
	s_cmpk_lg_u32 s96, 0x100
	s_mov_b32 s96, s44
	s_cbranch_scc1 .Lopx_5
	s_and_b32 s96, s44, 0xc0
	s_and_b32 s97, s44, 7
	s_lshl_b32 s97, s97, 3
	s_or_b32 s96, s96, s97
	s_bfe_u32 s97, s44, 0x30003
	s_or_b32 s96, s96, s97
.Lopx_5:
	s_cmpk_gt_i32 s96, 0x207
	s_cbranch_scc1 .LBB0_987
	v_lshlrev_b32_e32 v1, 3, v0
	s_add_u32 s0, s42, 0x628000
	v_and_b32_e32 v4, 24, v1
	s_addc_u32 s1, s43, 0
	s_lshl_b32 s5, s96, 5
	v_lshlrev_b32_e32 v102, 1, v4
	v_mov_b32_e32 v103, 0
	s_and_b32 s4, s5, 0xffffff00
	v_lshl_add_u64 v[2:3], s[42:43], 0, v[102:103]
	s_mov_b64 s[2:3], 0xf278000
	v_lshrrev_b32_e32 v114, 2, v0
	v_lshl_add_u64 v[104:105], v[2:3], 0, s[2:3]
	v_or_b32_e32 v2, s4, v114
	v_min_i32_e32 v2, 0x40ff, v2
	v_ashrrev_i32_e32 v3, 31, v2
	v_lshlrev_b64 v[2:3], 11, v[2:3]
	v_lshl_add_u64 v[106:107], v[104:105], 0, v[2:3]
	v_or_b32_e32 v2, 0x200, v0
	v_lshrrev_b32_e32 v115, 2, v2
	v_or_b32_e32 v2, s4, v115
	v_min_i32_e32 v2, 0x40ff, v2
	v_ashrrev_i32_e32 v3, 31, v2
	s_lshl_b32 s2, s96, 7
	v_lshlrev_b64 v[2:3], 11, v[2:3]
	s_and_b32 s2, s2, 0x380
	v_lshl_add_u64 v[108:109], v[104:105], 0, v[2:3]
	v_or_b32_e32 v2, s2, v114
	v_lshlrev_b32_e32 v2, 11, v2
	v_mov_b32_e32 v3, v103
	v_lshl_add_u64 v[2:3], s[0:1], 0, v[2:3]
	v_lshl_add_u64 v[110:111], v[2:3], 0, v[102:103]
	global_load_dwordx4 v[78:81], v[108:109], off
	global_load_dwordx4 v[90:93], v[108:109], off offset:64
	global_load_dwordx4 v[82:85], v[110:111], off
	global_load_dwordx4 v[94:97], v[110:111], off offset:64
	global_load_dwordx4 v[98:101], v[106:107], off offset:64
	global_load_dwordx4 v[66:69], v[106:107], off offset:128
	global_load_dwordx4 v[74:77], v[108:109], off offset:128
	global_load_dwordx4 v[86:89], v[106:107], off
	global_load_dwordx4 v[70:73], v[110:111], off offset:128
	v_mad_u32_u24 v3, v115, 40, v4
	v_mul_u32_u24_e32 v2, 40, v114
	v_lshl_add_u32 v117, v3, 1, 0
	v_lshrrev_b32_e32 v3, 1, v0
	v_add_lshl_u32 v2, v2, v4, 1
	v_and_b32_e32 v3, 0xc0, v3
	v_and_b32_e32 v4, 31, v0
	v_or_b32_e32 v5, v3, v4
	v_and_b32_e32 v6, 8, v114
	v_mul_u32_u24_e32 v5, 40, v5
	v_lshl_add_u32 v7, v6, 1, 0
	v_lshl_add_u32 v119, v5, 1, v7
	v_and_b32_e32 v5, 0x5f, v0
	v_mov_b32_e32 v11, 0x500
	v_mul_u32_u24_e32 v8, 0x50, v5
	v_mul_u32_u24_e32 v9, 40, v5
	v_mad_u32_u24 v5, v5, 40, v11
	v_add_lshl_u32 v10, v9, v6, 1
	v_add_lshl_u32 v11, v5, v6, 1
	v_or_b32_e32 v6, 16, v6
	s_add_i32 s2, 0, 0x11810
	v_add_lshl_u32 v12, v6, v9, 1
	v_add_lshl_u32 v5, v5, v6, 1
	v_add_u32_e32 v118, s2, v2
	v_add_u32_e32 v120, s2, v10
	v_add_u32_e32 v121, s2, v11
	v_add_u32_e32 v122, s2, v12
	v_add_u32_e32 v123, s2, v5
	s_add_i32 s2, 0, 0x14010
	v_add_u32_e32 v128, s2, v5
	v_lshrrev_b32_e32 v5, 3, v0
	v_add_u32_e32 v116, 0, v2
	v_add_u32_e32 v124, s2, v2
	v_and_b32_e32 v2, 64, v0
	v_and_or_b32 v3, v5, 4, v3
	v_lshl_add_u32 v2, v2, 2, 0
	v_lshlrev_b32_e32 v4, 2, v4
	v_mul_u32_u24_e32 v3, 0x210, v3
	v_add3_u32 v131, v2, v4, v3
	v_and_b32_e32 v2, 15, v0
	v_add_u32_e32 v125, s2, v10
	v_add_u32_e32 v126, s2, v11
	v_add_u32_e32 v127, s2, v12
	s_movk_i32 s2, 0x210
	v_lshrrev_b32_e32 v133, 4, v0
	v_lshlrev_b32_e32 v2, 5, v2
	v_mad_u32_u24 v2, v133, s2, v2
	v_readlane_b32 s2, v253, 10
	v_lshl_add_u64 v[112:113], s[0:1], 0, v[102:103]
	s_add_u32 s0, s42, 0x112f8000
	v_readlane_b32 s3, v253, 11
	v_lshl_add_u32 v129, v9, 1, v7
	v_add_u32_e32 v130, 0, v12
	s_addc_u32 s1, s43, 0
	v_or_b32_e32 v132, 0xfffffe00, v0
	v_add3_u32 v134, v2, 0, 16
	s_lshl_b32 s14, s2, 5
	v_add_u32_e32 v135, v7, v8
	s_movk_i32 s15, 0x4100
	s_movk_i32 s16, 0x100
	s_mov_b64 s[2:3], 0x12000
	s_mov_b32 s17, 0x12000
	s_mov_b32 s4, 0x3fb504f3
	s_movk_i32 s18, 0xdff
	s_mov_b32 s8, s96
	s_branch .LBB0_977

; __device__ __forceinline__ void phase_outproj(const Params& P, int layer, bfr* smem, int bid, int nb) {
;     ...
;     const int mt = (M + 255) / 256, nu = mt * 8;
;     GemmPipe<256, 128, 1024, ALoadRows, BLoadT> gp;
;     ALoadRows al; BLoadT bl;
;     int u = bid;
;     if (u < nu) { al.init<256>(A, 1024, m0 + (u >> 3) * 256, NT - 1, nullptr); bl.init<128>(Bt, 1024, (u & 7) * 128); gp.prefetch(al, bl); }
;     while (u < nu) {
;         EpiOutProj ep{xc, xl, x2, mod, (bfr*)(P.ws + WS_PRE), m0 + (u >> 3) * 256, (u & 7) * 128};
;         gp.mainloop(smem, al, bl);
;         const int un = u + nb;
;         if (un < nu) { al.init<256>(A, 1024, m0 + (un >> 3) * 256, NT - 1, nullptr); bl.init<128>(Bt, 1024, (un & 7) * 128); gp.prefetch(al, bl); }
.LBB0_2118:
	s_cmp_lt_i32 s6, 16
	s_cselect_b64 s[0:1], -1, 0
	s_cmp_gt_i32 s7, 15
	s_cselect_b64 s[2:3], -1, 0
	s_and_b64 s[0:1], s[0:1], s[2:3]
	s_andn2_b64 vcc, exec, s[0:1]
	s_cbranch_vccnz .LBB0_2182
	v_readlane_b32 s96, v253, 10
	s_cmpk_lg_u32 s96, 0x100
	s_mov_b32 s96, s44
	s_cbranch_scc1 .Lopx_15
	s_and_b32 s96, s44, 0xc0
	s_and_b32 s97, s44, 7
	s_lshl_b32 s97, s97, 3
	s_or_b32 s96, s96, s97
	s_bfe_u32 s97, s44, 0x30003
	s_or_b32 s96, s96, s97
.Lopx_15:
	s_cmpk_gt_i32 s96, 0x1ff
	s_cbranch_scc1 .LBB0_2128
	s_add_u32 s0, s42, 0x1b578000
	s_addc_u32 s1, s43, 0
	s_add_u32 s2, s42, 0xaa8000
	v_lshlrev_b32_e32 v1, 3, v0
	s_addc_u32 s3, s43, 0
	s_lshl_b32 s7, s96, 5
	v_and_b32_e32 v4, 24, v1
	s_and_b32 s4, s7, 0xffffff00
	s_waitcnt vmcnt(4)
	v_lshlrev_b32_e32 v102, 1, v4
	v_mov_b32_e32 v103, 0
	s_add_i32 s6, s4, 0x100
	s_waitcnt lgkmcnt(1)
	v_lshl_add_u64 v[2:3], s[42:43], 0, v[102:103]
	s_mov_b64 s[4:5], 0xf278000
	v_lshrrev_b32_e32 v116, 2, v0
	v_lshl_add_u64 v[104:105], v[2:3], 0, s[4:5]
	v_or_b32_e32 v2, s6, v116
	v_min_i32_e32 v2, 0x40ff, v2
	v_ashrrev_i32_e32 v3, 31, v2
	v_lshlrev_b64 v[2:3], 11, v[2:3]
	v_lshl_add_u64 v[106:107], v[104:105], 0, v[2:3]
	v_or_b32_e32 v2, 0x200, v0
	v_lshrrev_b32_e32 v117, 2, v2
	v_or_b32_e32 v2, s6, v117
	v_min_i32_e32 v2, 0x40ff, v2
	v_ashrrev_i32_e32 v3, 31, v2
	s_lshl_b32 s4, s96, 7
	v_lshlrev_b64 v[2:3], 11, v[2:3]
	s_and_b32 s4, s4, 0x380
	v_lshl_add_u64 v[108:109], v[104:105], 0, v[2:3]
	v_or_b32_e32 v2, s4, v116
	v_lshlrev_b32_e32 v2, 11, v2
	v_mov_b32_e32 v3, v103
	v_lshl_add_u64 v[2:3], s[2:3], 0, v[2:3]
	v_lshl_add_u64 v[110:111], v[2:3], 0, v[102:103]
	global_load_dwordx4 v[78:81], v[108:109], off
	global_load_dwordx4 v[90:93], v[108:109], off offset:64
	global_load_dwordx4 v[82:85], v[110:111], off
	global_load_dwordx4 v[94:97], v[110:111], off offset:64
	global_load_dwordx4 v[98:101], v[106:107], off offset:64
	global_load_dwordx4 v[66:69], v[106:107], off offset:128
	global_load_dwordx4 v[74:77], v[108:109], off offset:128
	global_load_dwordx4 v[86:89], v[106:107], off
	global_load_dwordx4 v[70:73], v[110:111], off offset:128
	v_mad_u32_u24 v3, v117, 40, v4
	v_mul_u32_u24_e32 v2, 40, v116
	v_lshl_add_u32 v119, v3, 1, 0
	v_lshrrev_b32_e32 v3, 1, v0
	v_add_lshl_u32 v2, v2, v4, 1
	v_and_b32_e32 v3, 0xc0, v3
	v_and_b32_e32 v4, 31, v0
	s_waitcnt lgkmcnt(0)
	v_or_b32_e32 v5, v3, v4
	v_and_b32_e32 v6, 8, v116
	v_mul_u32_u24_e32 v5, 40, v5
	v_lshl_add_u32 v7, v6, 1, 0
	v_lshl_add_u32 v121, v5, 1, v7
	v_and_b32_e32 v5, 0x5f, v0
	v_mov_b32_e32 v11, 0x500
	v_mul_u32_u24_e32 v8, 0x50, v5
	v_mul_u32_u24_e32 v9, 40, v5
	v_mad_u32_u24 v5, v5, 40, v11
	v_add_lshl_u32 v10, v9, v6, 1
	v_add_lshl_u32 v11, v5, v6, 1
	v_or_b32_e32 v6, 16, v6
	s_add_i32 s4, 0, 0x11810
	v_add_lshl_u32 v12, v6, v9, 1
	v_add_lshl_u32 v5, v5, v6, 1
	v_add_u32_e32 v120, s4, v2
	v_add_u32_e32 v122, s4, v10
	v_add_u32_e32 v123, s4, v11
	v_add_u32_e32 v124, s4, v12
	v_add_u32_e32 v125, s4, v5
	s_add_i32 s4, 0, 0x14010
	s_waitcnt vmcnt(9)
	v_add_u32_e32 v130, s4, v5
	v_lshrrev_b32_e32 v5, 3, v0
	v_add_u32_e32 v118, 0, v2
	v_add_u32_e32 v126, s4, v2
	v_and_b32_e32 v2, 64, v0
	v_and_or_b32 v3, v5, 4, v3
	v_lshl_add_u32 v2, v2, 2, 0
	v_lshlrev_b32_e32 v4, 2, v4
	v_mul_u32_u24_e32 v3, 0x210, v3
	v_add3_u32 v133, v2, v4, v3
	v_and_b32_e32 v3, 15, v0
	v_add_u32_e32 v127, s4, v10
	v_add_u32_e32 v128, s4, v11
	v_add_u32_e32 v129, s4, v12
	s_movk_i32 s4, 0x210
	v_lshrrev_b32_e32 v2, 4, v0
	v_lshlrev_b32_e32 v3, 5, v3
	v_mad_u32_u24 v3, v2, s4, v3
	v_readlane_b32 s4, v253, 10
	v_lshl_add_u64 v[112:113], s[2:3], 0, v[102:103]
	s_add_u32 s2, s42, 0x112f8000
	v_readlane_b32 s5, v253, 11
	v_lshl_add_u32 v131, v9, 1, v7
	v_add_u32_e32 v132, 0, v12
	s_addc_u32 s3, s43, 0
	v_or_b32_e32 v134, 0xfffffe00, v0
	v_add3_u32 v135, v3, 0, 16
	v_or_b32_e32 v136, 0x100, v2
	s_lshl_b32 s14, s4, 5
	v_add_u32_e32 v137, v7, v8
	s_movk_i32 s15, 0x4100
	s_movk_i32 s16, 0xff
	s_mov_b64 s[4:5], 0x1e000
	s_mov_b32 s17, 0x1e000
	s_mov_b32 s6, 0x3fb504f3
	s_movk_i32 s18, 0xdff
	v_mov_b32_e32 v138, 0x6000
	s_mov_b32 s10, s96
	s_branch .LBB0_2122
